# v13 + moba_c: per-list entry counts kept in LDS instead of a global load per item
# baseline (speedup 1.0000x reference)
.LBB0_1321:
	s_movk_i32 s0, 0x100
	v_cmp_gt_u32_e64 s[0:1], s0, v0
	v_mov_b32_e32 v1, 0
	s_and_saveexec_b64 s[4:5], s[0:1]
	s_cbranch_execz .LBB0_1325
	s_waitcnt lgkmcnt(0)
	v_lshlrev_b32_e32 v2, 2, v0
	v_mov_b32_e32 v3, 0
	v_lshl_add_u64 v[2:3], s[46:47], 0, v[2:3]
	v_add_co_u32_e32 v2, vcc, 0x1000, v2
	s_nop 1
	v_addc_co_u32_e32 v3, vcc, 0, v3, vcc
	global_load_dword v1, v[2:3], off sc1
	v_mbcnt_lo_u32_b32 v2, -1, 0
	v_mbcnt_hi_u32_b32 v2, -1, v2
	v_and_b32_e32 v3, 64, v2
	v_add_u32_e32 v4, -1, v2
	v_cmp_lt_i32_e32 vcc, v4, v3
	v_add_u32_e32 v5, -2, v2
	v_add_u32_e32 v6, -4, v2
	v_cndmask_b32_e32 v4, v4, v2, vcc
	v_lshlrev_b32_e32 v4, 2, v4
	v_cmp_lt_i32_e32 vcc, v5, v3
	v_add_u32_e32 v7, -8, v2
	v_add_u32_e32 v8, -16, v2
	v_cndmask_b32_e32 v5, v5, v2, vcc
	v_cmp_ne_u32_e32 vcc, 0, v248
	v_lshlrev_b32_e32 v5, 2, v5
	v_subrev_u32_e32 v9, 32, v2
	s_waitcnt vmcnt(0)
	v_lshlrev_b32_e32 v10, 2, v0
	v_add_u32_e32 v10, 0x21800, v10
	ds_write_b32 v10, v1
	v_add_u32_e32 v1, 0xff, v1
	v_ashrrev_i32_e32 v1, 8, v1
	ds_bpermute_b32 v4, v4, v1
	s_waitcnt lgkmcnt(0)
	v_cndmask_b32_e32 v4, 0, v4, vcc
	v_add_u32_e32 v4, v4, v1
	ds_bpermute_b32 v5, v5, v4
	v_cmp_lt_i32_e32 vcc, v6, v3
	s_nop 1
	v_cndmask_b32_e32 v6, v6, v2, vcc
	v_cmp_lt_u32_e32 vcc, 1, v248
	v_lshlrev_b32_e32 v6, 2, v6
	s_waitcnt lgkmcnt(0)
	v_cndmask_b32_e32 v5, 0, v5, vcc
	v_add_u32_e32 v4, v5, v4
	ds_bpermute_b32 v5, v6, v4
	v_cmp_lt_i32_e32 vcc, v7, v3
	s_nop 1
	v_cndmask_b32_e32 v6, v7, v2, vcc
	v_cmp_lt_u32_e32 vcc, 3, v248
	v_lshlrev_b32_e32 v6, 2, v6
	s_waitcnt lgkmcnt(0)
	v_cndmask_b32_e32 v5, 0, v5, vcc
	v_add_u32_e32 v4, v5, v4
	ds_bpermute_b32 v5, v6, v4
	v_cmp_lt_i32_e32 vcc, v8, v3
	s_nop 1
	v_cndmask_b32_e32 v6, v8, v2, vcc
	v_cmp_lt_u32_e32 vcc, 7, v248
	v_lshlrev_b32_e32 v6, 2, v6
	s_waitcnt lgkmcnt(0)
	v_cndmask_b32_e32 v5, 0, v5, vcc
	v_add_u32_e32 v4, v5, v4
	ds_bpermute_b32 v5, v6, v4
	v_cmp_lt_i32_e32 vcc, v9, v3
	s_nop 1
	v_cndmask_b32_e32 v2, v9, v2, vcc
	v_cmp_lt_u32_e32 vcc, 15, v248
	v_lshlrev_b32_e32 v2, 2, v2
	s_waitcnt lgkmcnt(0)
	v_cndmask_b32_e32 v3, 0, v5, vcc
	v_add_u32_e32 v3, v3, v4
	ds_bpermute_b32 v2, v2, v3
	v_cmp_lt_u32_e32 vcc, 31, v248
	s_waitcnt lgkmcnt(0)
	s_nop 0
	v_cndmask_b32_e32 v2, 0, v2, vcc
	v_add_u32_e32 v2, v2, v3
	v_cmp_eq_u32_e32 vcc, 63, v248
	s_and_saveexec_b64 s[6:7], vcc
	s_lshl_b32 s8, s91, 2
	s_add_i32 s8, s8, 0
	s_add_i32 s8, s8, 0x21410
	v_mov_b32_e32 v3, s8
	ds_write_b32 v3, v2
	s_or_b64 exec, exec, s[6:7]
	v_lshl_add_u32 v3, v0, 2, 0
	v_sub_u32_e32 v2, v2, v1
	v_add_u32_e32 v3, 0x21000, v3
	ds_write_b32 v3, v2

.LBB0_1366:
	s_add_i32 s1, s10, s0
	s_add_i32 s1, s1, 1
	s_ashr_i32 s1, s1, 1
	s_lshl_b32 s4, s1, 2
	s_add_i32 s4, s4, 0
	s_add_i32 s4, s4, 0x21000
	v_mov_b32_e32 v6, s4
	ds_read_b32 v6, v6
	s_add_i32 s4, s1, -1
	s_waitcnt lgkmcnt(0)
	v_readfirstlane_b32 s5, v6
	s_cmp_gt_i32 s5, s6
	s_cselect_b32 s0, s4, s0
	s_cselect_b32 s10, s10, s1
	s_cmp_lt_i32 s10, s0
	s_cbranch_scc1 .LBB0_1366
	s_lshl_b32 s0, s10, 2
	s_add_i32 s0, s0, 0
	s_add_i32 s0, s0, 0x21000
	s_add_u32 s7, s46, 0x1000
	s_addc_u32 s9, s47, 0
	s_ashr_i32 s11, s10, 31
	v_mov_b32_e32 v6, s0
	s_lshl_b64 s[0:1], s[10:11], 2
	s_add_u32 s0, s7, s0
	s_addc_u32 s1, s9, s1
	v_mov_b32_e32 v148, 0
	ds_read_b32 v7, v6
	ds_read_b32 v6, v6 offset:2048
	s_lshl_b32 s26, s91, 5
	s_waitcnt lgkmcnt(0)
	v_sub_u32_e32 v7, s6, v7
	v_lshlrev_b32_e32 v7, 8, v7
	v_add_u32_e32 v7, s26, v7
	s_waitcnt vmcnt(0)
	v_cmp_lt_i32_e64 s[24:25], v7, v6
	s_and_b64 vcc, exec, s[24:25]
	s_cbranch_vccnz .LBB0_1372
	v_lshlrev_b32_e32 v146, 3, v157
	v_mov_b32_e32 v147, 0
	s_cbranch_execz .LBB0_1373
	v_mov_b32_e32 v82, 0
	v_mov_b32_e32 v84, v82
	v_mov_b32_e32 v85, v82
	v_mov_b32_e32 v83, v82
	v_mov_b64_e32 v[88:89], v[84:85]
	v_mov_b64_e32 v[92:93], v[84:85]
	v_mov_b64_e32 v[96:97], v[84:85]
	v_mov_b64_e32 v[100:101], v[84:85]
	v_mov_b64_e32 v[104:105], v[84:85]
	v_mov_b64_e32 v[108:109], v[84:85]
	v_mov_b64_e32 v[112:113], v[84:85]
	s_mov_b64 s[14:15], 0
	v_mov_b64_e32 v[86:87], v[82:83]
	v_mov_b64_e32 v[90:91], v[82:83]
	v_mov_b64_e32 v[94:95], v[82:83]
	v_mov_b64_e32 v[98:99], v[82:83]
	v_mov_b64_e32 v[102:103], v[82:83]
	v_mov_b64_e32 v[106:107], v[82:83]
	v_mov_b64_e32 v[110:111], v[82:83]
	v_mov_b32_e32 v155, 0
	s_branch .LBB0_1374

.LBB0_1383:
	s_add_i32 s20, s10, s11
	s_add_i32 s20, s20, 1
	s_ashr_i32 s20, s20, 1
	s_lshl_b32 s21, s20, 2
	s_add_i32 s21, s21, 0
	s_add_i32 s21, s21, 0x21000
	v_mov_b32_e32 v2, s21
	ds_read_b32 v2, v2
	s_add_i32 s21, s20, -1
	s_waitcnt lgkmcnt(0)
	v_readfirstlane_b32 s22, v2
	s_cmp_gt_i32 s22, s6
	s_cselect_b32 s11, s21, s11
	s_cselect_b32 s10, s10, s20
	s_cmp_lt_i32 s10, s11
	s_cbranch_scc1 .LBB0_1383
	s_lshl_b32 s11, s10, 2
	s_add_i32 s11, s11, 0
	s_add_i32 s11, s11, 0x21000
	v_mov_b32_e32 v2, s11
	s_ashr_i32 s11, s10, 31
	s_lshl_b64 s[20:21], s[10:11], 2
	s_add_u32 s20, s7, s20
	s_addc_u32 s21, s9, s21
	v_mov_b32_e32 v151, 0
	ds_read_b32 v3, v2
	ds_read_b32 v2, v2 offset:2048
	s_waitcnt vmcnt(2)
	v_mov_b64_e32 v[116:117], v[112:113]
	v_mov_b64_e32 v[120:121], v[108:109]
	v_mov_b64_e32 v[124:125], v[104:105]
	s_waitcnt lgkmcnt(0)
	v_sub_u32_e32 v3, s6, v3
	v_lshlrev_b32_e32 v3, 8, v3
	v_add_u32_e32 v3, s26, v3
	v_mov_b64_e32 v[128:129], v[100:101]
	v_mov_b64_e32 v[132:133], v[96:97]
	v_mov_b64_e32 v[136:137], v[92:93]
	v_mov_b64_e32 v[140:141], v[88:89]
	s_waitcnt vmcnt(1)
	v_mov_b64_e32 v[144:145], v[84:85]
	s_mov_b64 s[20:21], 0
	s_mov_b64 s[22:23], 0
	v_mov_b32_e32 v153, 0
	v_mov_b64_e32 v[114:115], v[110:111]
	v_mov_b64_e32 v[118:119], v[106:107]
	v_mov_b64_e32 v[122:123], v[102:103]
	v_mov_b64_e32 v[126:127], v[98:99]
	v_mov_b64_e32 v[130:131], v[94:95]
	v_mov_b64_e32 v[134:135], v[90:91]
	v_mov_b64_e32 v[138:139], v[86:87]
	v_mov_b64_e32 v[142:143], v[82:83]
	s_waitcnt vmcnt(0)
	v_cmp_ge_i32_e32 vcc, v3, v2
	s_cbranch_vccnz .LBB0_1387
	s_and_b32 s11, s10, 63
	s_add_i32 s23, s11, -1
	s_mul_i32 s22, s11, 63
	s_mul_i32 s11, s23, s11
	s_lshr_b32 s23, s11, 31
	s_add_i32 s11, s11, s23
	s_sext_i32_i16 s11, s11
	s_lshr_b32 s11, s11, 1
	s_sub_i32 s11, 0, s11
	s_sext_i32_i16 s11, s11
	s_ashr_i32 s20, s10, 6
	v_or_b32_e32 v4, v3, v156
	s_add_i32 s22, s22, s11
	s_mul_i32 s21, s20, 0x7e000
	s_lshl_b32 s11, s22, 8
	v_cmp_lt_i32_e32 vcc, v4, v2
	s_add_i32 s11, s11, s21
	s_ashr_i32 s21, s20, 31
	v_cndmask_b32_e32 v2, v3, v4, vcc
	v_add_u32_e32 v2, s11, v2
	v_ashrrev_i32_e32 v3, 31, v2
	v_lshl_add_u64 v[2:3], v[2:3], 2, s[12:13]
	global_load_dword v4, v[2:3], off
	s_lshl_b64 s[20:21], s[20:21], 22
	s_add_u32 s20, s27, s20
	v_mov_b32_e32 v3, v149
	s_addc_u32 s21, s28, s21
	s_mov_b64 s[22:23], -1
	s_waitcnt vmcnt(0)
	v_and_b32_e32 v153, 0xffff, v4
	v_lshlrev_b32_e32 v2, 8, v153
	v_lshl_add_u64 v[2:3], s[20:21], 0, v[2:3]
	v_lshl_add_u64 v[2:3], v[146:147], 1, v[2:3]
	global_load_dwordx4 v[114:117], v[2:3], off
	global_load_dwordx4 v[118:121], v[2:3], off offset:32
	global_load_dwordx4 v[122:125], v[2:3], off offset:64
	global_load_dwordx4 v[126:129], v[2:3], off offset:96
	global_load_dwordx4 v[130:133], v[2:3], off offset:128
	global_load_dwordx4 v[134:137], v[2:3], off offset:160
	global_load_dwordx4 v[138:141], v[2:3], off offset:192
	global_load_dwordx4 v[142:145], v[2:3], off offset:224
	v_lshrrev_b32_e32 v151, 16, v4
	s_and_b64 s[20:21], vcc, exec
	s_branch .LBB0_1387
